# variant D with the whole kernel shifted by 32 bytes (8 s_nop at entry): code-placement test
# baseline (speedup 1.0000x reference)
_Z3fwd4Args:
	s_nop 0
	s_nop 0
	s_nop 0
	s_nop 0
	s_nop 0
	s_nop 0
	s_nop 0
	s_nop 0
	v_lshl_add_u32 v1, v0, 2, 0
	v_add_u32_e32 v1, 0x20000, v1
	v_mov_b32_e32 v2, 0
	s_mov_b32 s10, s2
	ds_write2st64_b32 v1, v2, v2 offset1:8
	ds_write2st64_b32 v1, v2, v2 offset0:16 offset1:24
	v_or_b32_e32 v1, 0x800, v0
	s_mov_b64 s[2:3], -1
	s_and_saveexec_b64 s[4:5], s[2:3]
	v_lshl_add_u32 v3, v1, 2, 0
	v_add_u32_e32 v3, 0x20000, v3
	ds_write_b32 v3, v2
	s_or_b64 exec, exec, s[4:5]
	s_and_saveexec_b64 s[4:5], s[2:3]
	s_add_i32 s2, 0, 0x20000
	v_lshl_add_u32 v1, v1, 2, s2
	v_mov_b32_e32 v2, 0
	ds_write_b32 v1, v2 offset:2048
	s_or_b64 exec, exec, s[4:5]
	v_or_b32_e32 v1, 0xc00, v0
	v_cmp_gt_u32_e64 s[2:3], 7, 6
	v_cmp_gt_u32_e64 s[6:7], 7, 5
	s_and_saveexec_b64 s[4:5], s[6:7]
	v_lshl_add_u32 v2, v1, 2, 0
	v_add_u32_e32 v2, 0x20000, v2
	v_mov_b32_e32 v3, 0
	ds_write_b32 v2, v3
	s_or_b64 exec, exec, s[4:5]
	s_and_saveexec_b64 s[4:5], s[2:3]
	s_add_i32 s2, 0, 0x20000
	v_lshl_add_u32 v1, v1, 2, s2
	v_mov_b32_e32 v2, 0
	ds_write_b32 v1, v2 offset:2048
	s_or_b64 exec, exec, s[4:5]
	v_cmp_eq_u32_e32 vcc, 0, v0
	s_waitcnt lgkmcnt(0)
	s_barrier
	s_and_saveexec_b64 s[2:3], vcc
	s_cbranch_execz .LBB0_10
	s_load_dwordx16 s[12:27], s[0:1], 0x0
	s_add_i32 s4, 0, 0x201c0
	s_load_dwordx16 s[36:51], s[0:1], 0x40
	v_mov_b32_e32 v1, s4
	s_add_i32 s4, 0, 0x201d0
	s_waitcnt lgkmcnt(0)
	v_mov_b32_e32 v2, s12
	v_mov_b32_e32 v3, s13
	v_mov_b32_e32 v4, s14
	v_mov_b32_e32 v5, s15
	ds_write_b128 v1, v[2:5]
	v_mov_b32_e32 v2, s16
	v_mov_b32_e32 v3, s17
	v_mov_b32_e32 v4, s18
	v_mov_b32_e32 v5, s19
	v_mov_b32_e32 v1, s4
	s_add_i32 s4, 0, 0x201e0
	ds_write_b128 v1, v[2:5]
	v_mov_b32_e32 v2, s20
	v_mov_b32_e32 v3, s21
	v_mov_b32_e32 v4, s22
	v_mov_b32_e32 v5, s23
	v_mov_b32_e32 v1, s4
	s_add_i32 s4, 0, 0x201f0
	ds_write_b128 v1, v[2:5]
	v_mov_b32_e32 v2, s24
	v_mov_b32_e32 v3, s25
	v_mov_b32_e32 v4, s26
	v_mov_b32_e32 v5, s27
	v_mov_b32_e32 v1, s4
	s_add_i32 s4, 0, 0x20200
	s_load_dwordx16 s[12:27], s[0:1], 0x80
	ds_write_b128 v1, v[2:5]
	v_mov_b32_e32 v2, s36
	v_mov_b32_e32 v3, s37
	v_mov_b32_e32 v4, s38
	v_mov_b32_e32 v5, s39
	v_mov_b32_e32 v1, s4
	s_add_i32 s4, 0, 0x20210
	ds_write_b128 v1, v[2:5]
	v_mov_b32_e32 v2, s40
	v_mov_b32_e32 v3, s41
	v_mov_b32_e32 v4, s42
	v_mov_b32_e32 v5, s43
	v_mov_b32_e32 v1, s4
	s_add_i32 s4, 0, 0x20220
	ds_write_b128 v1, v[2:5]
	v_mov_b32_e32 v2, s44
	v_mov_b32_e32 v3, s45
	v_mov_b32_e32 v4, s46
	v_mov_b32_e32 v5, s47
	v_mov_b32_e32 v1, s4
	s_add_i32 s4, 0, 0x20230
	ds_write_b128 v1, v[2:5]
	v_mov_b32_e32 v2, s48
	v_mov_b32_e32 v3, s49
	v_mov_b32_e32 v4, s50
	v_mov_b32_e32 v5, s51
	v_mov_b32_e32 v1, s4
	s_add_i32 s4, 0, 0x20240
	ds_write_b128 v1, v[2:5]
	s_waitcnt lgkmcnt(0)
	v_mov_b32_e32 v2, s12
	v_mov_b32_e32 v3, s13
	v_mov_b32_e32 v4, s14
	v_mov_b32_e32 v5, s15
	v_mov_b32_e32 v1, s4
	s_add_i32 s4, 0, 0x20250
	ds_write_b128 v1, v[2:5]
	v_mov_b32_e32 v2, s16
	v_mov_b32_e32 v3, s17
	v_mov_b32_e32 v4, s18
	v_mov_b32_e32 v5, s19
	v_mov_b32_e32 v1, s4
	s_add_i32 s4, 0, 0x20260
	ds_write_b128 v1, v[2:5]
	v_mov_b32_e32 v1, s4
	s_load_dwordx2 s[4:5], s[0:1], 0xc0
	v_mov_b32_e32 v2, s20
	v_mov_b32_e32 v3, s21
	v_mov_b32_e32 v4, s22
	v_mov_b32_e32 v5, s23
	s_add_i32 s6, 0, 0x20270
	ds_write_b128 v1, v[2:5]
	v_mov_b32_e32 v2, s24
	v_mov_b32_e32 v3, s25
	v_mov_b32_e32 v4, s26
	v_mov_b32_e32 v5, s27
	v_mov_b32_e32 v1, s6
	s_add_i32 s6, 0, 0x20280
	ds_write_b128 v1, v[2:5]
	v_mov_b32_e32 v1, s6
	s_waitcnt lgkmcnt(0)
	v_mov_b64_e32 v[2:3], s[4:5]
	ds_write_b64 v1, v[2:3]
